# speedup vs baseline: 1.0071x; 1.0010x over previous
.LBB0_23:
	s_andn2_b64 vcc, exec, s[4:5]
	s_cbranch_vccnz .LBB0_43
	s_load_dwordx2 s[4:5], s[0:1], 0x0
	s_add_i32 s3, s2, 0xfffffdd6
	s_ashr_i32 s76, s3, 4
	v_lshlrev_b32_e32 v43, 3, v31
	v_lshl_or_b32 v2, s76, 5, v43
	v_lshrrev_b32_e32 v42, 8, v0
	s_lshl_b32 s3, s3, 1
	v_ashrrev_i32_e32 v3, 31, v2
	v_and_or_b32 v1, s3, 30, v42
	v_lshlrev_b64 v[2:3], 15, v[2:3]
	s_waitcnt lgkmcnt(0)
	v_lshl_add_u64 v[2:3], s[4:5], 0, v[2:3]
	v_lshlrev_b32_e32 v38, 10, v1
	v_mov_b32_e32 v39, 0
	v_lshl_add_u64 v[2:3], v[2:3], 0, v[38:39]
	v_lshlrev_b32_e32 v38, 4, v30
	v_lshl_add_u64 v[2:3], v[2:3], 0, v[38:39]
	s_mov_b32 s3, 0x8000
	v_add_co_u32_e32 v4, vcc, s3, v2
	s_mov_b32 s3, 0x10000
	s_nop 0
	v_addc_co_u32_e32 v5, vcc, 0, v3, vcc
	global_load_dwordx4 v[34:37], v[2:3], off nt
	global_load_dwordx4 v[26:29], v[4:5], off nt
	v_add_co_u32_e32 v4, vcc, s3, v2
	s_mov_b32 s3, 0x18000
	s_nop 0
	v_addc_co_u32_e32 v5, vcc, 0, v3, vcc
	v_add_co_u32_e32 v6, vcc, s3, v2
	s_mov_b32 s3, 0x20000
	s_nop 0
	v_addc_co_u32_e32 v7, vcc, 0, v3, vcc
	global_load_dwordx4 v[22:25], v[4:5], off nt
	global_load_dwordx4 v[18:21], v[6:7], off nt
	v_add_co_u32_e32 v4, vcc, s3, v2
	s_mov_b32 s3, 0x28000
	s_nop 0
	v_addc_co_u32_e32 v5, vcc, 0, v3, vcc
	v_add_co_u32_e32 v6, vcc, s3, v2
	s_mov_b32 s3, 0x30000
	s_nop 0
	v_addc_co_u32_e32 v7, vcc, 0, v3, vcc
	v_add_co_u32_e32 v32, vcc, s3, v2
	s_mov_b32 s3, 0x38000
	s_nop 0
	v_addc_co_u32_e32 v33, vcc, 0, v3, vcc
	v_add_co_u32_e32 v40, vcc, s3, v2
	global_load_dwordx4 v[14:17], v[4:5], off nt
	global_load_dwordx4 v[10:13], v[6:7], off nt
	v_addc_co_u32_e32 v41, vcc, 0, v3, vcc
	global_load_dwordx4 v[6:9], v[32:33], off nt
	global_load_dwordx4 v[2:5], v[40:41], off nt
	v_mbcnt_lo_u32_b32 v33, -1, 0
	v_mbcnt_hi_u32_b32 v33, -1, v33
	v_and_b32_e32 v40, 64, v33
	v_xor_b32_e32 v39, 1, v33
	v_add_u32_e32 v40, 64, v40
	v_cmp_lt_i32_e32 vcc, v39, v40
	v_mov_b32_e32 v32, 0x800
	v_lshl_or_b32 v32, v42, 10, v32
	v_cndmask_b32_e32 v33, v33, v39, vcc
	v_lshlrev_b32_e32 v33, 2, v33
	s_waitcnt vmcnt(7)
	v_cmp_neq_f32_e32 vcc, 0, v34
	s_nop 1
	v_cndmask_b32_e64 v34, 0, 1, vcc
	v_cmp_neq_f32_e32 vcc, 0, v35
	s_nop 1
	v_cndmask_b32_e64 v35, 0, 2, vcc
	v_cmp_neq_f32_e32 vcc, 0, v36
	v_or_b32_e32 v34, v35, v34
	s_nop 0
	v_cndmask_b32_e64 v36, 0, 4, vcc
	v_cmp_neq_f32_e32 vcc, 0, v37
	s_nop 1
	v_cndmask_b32_e64 v35, 0, 8, vcc
	v_or3_b32 v35, v34, v36, v35
	s_nop 1
	v_mov_b32_dpp v36, v35 quad_perm:[1,0,3,2] row_mask:0xf bank_mask:0xf
	v_and_b32_e32 v34, 1, v0
	v_cmp_eq_u32_e32 vcc, 0, v34
	v_or_b32_e32 v34, v32, v43
	v_add_u32_e32 v34, v34, v38
	v_lshl_or_b32 v35, v36, 4, v35
	v_mov_b32_e32 v44, v35
	s_waitcnt vmcnt(6)
	v_cmp_neq_f32_e64 s[4:5], 0, v26
	s_nop 1
	v_cndmask_b32_e64 v26, 0, 1, s[4:5]
	v_cmp_neq_f32_e64 s[4:5], 0, v27
	s_nop 1
	v_cndmask_b32_e64 v27, 0, 2, s[4:5]
	v_cmp_neq_f32_e64 s[4:5], 0, v28
	v_or_b32_e32 v26, v27, v26
	s_nop 0
	v_cndmask_b32_e64 v27, 0, 4, s[4:5]
	v_cmp_neq_f32_e64 s[4:5], 0, v29
	s_nop 1
	v_cndmask_b32_e64 v28, 0, 8, s[4:5]
	v_or3_b32 v26, v26, v27, v28
	s_nop 1
	v_mov_b32_dpp v27, v26 quad_perm:[1,0,3,2] row_mask:0xf bank_mask:0xf
	v_lshl_or_b32 v26, v27, 4, v26
	v_lshl_or_b32 v44, v26, 8, v44
	s_waitcnt vmcnt(5)
	v_cmp_neq_f32_e64 s[4:5], 0, v22
	s_nop 1
	v_cndmask_b32_e64 v22, 0, 1, s[4:5]
	v_cmp_neq_f32_e64 s[4:5], 0, v23
	s_nop 1
	v_cndmask_b32_e64 v23, 0, 2, s[4:5]
	v_cmp_neq_f32_e64 s[4:5], 0, v24
	v_or_b32_e32 v22, v23, v22
	s_nop 0
	v_cndmask_b32_e64 v23, 0, 4, s[4:5]
	v_cmp_neq_f32_e64 s[4:5], 0, v25
	s_nop 1
	v_cndmask_b32_e64 v24, 0, 8, s[4:5]
	v_or3_b32 v22, v22, v23, v24
	s_nop 1
	v_mov_b32_dpp v23, v22 quad_perm:[1,0,3,2] row_mask:0xf bank_mask:0xf
	v_lshl_or_b32 v22, v23, 4, v22
	v_lshl_or_b32 v44, v22, 16, v44
	s_waitcnt vmcnt(4)
	v_cmp_neq_f32_e64 s[4:5], 0, v18
	s_nop 1
	v_cndmask_b32_e64 v18, 0, 1, s[4:5]
	v_cmp_neq_f32_e64 s[4:5], 0, v19
	s_nop 1
	v_cndmask_b32_e64 v19, 0, 2, s[4:5]
	v_cmp_neq_f32_e64 s[4:5], 0, v20
	v_or_b32_e32 v18, v19, v18
	s_nop 0
	v_cndmask_b32_e64 v19, 0, 4, s[4:5]
	v_cmp_neq_f32_e64 s[4:5], 0, v21
	s_nop 1
	v_cndmask_b32_e64 v20, 0, 8, s[4:5]
	v_or3_b32 v18, v18, v19, v20
	s_nop 1
	v_mov_b32_dpp v19, v18 quad_perm:[1,0,3,2] row_mask:0xf bank_mask:0xf
	v_lshl_or_b32 v18, v19, 4, v18
	v_lshl_or_b32 v44, v18, 24, v44
	s_waitcnt vmcnt(3)
	v_cmp_neq_f32_e64 s[4:5], 0, v14
	s_nop 1
	v_cndmask_b32_e64 v14, 0, 1, s[4:5]
	v_cmp_neq_f32_e64 s[4:5], 0, v15
	s_nop 1
	v_cndmask_b32_e64 v15, 0, 2, s[4:5]
	v_cmp_neq_f32_e64 s[4:5], 0, v16
	v_or_b32_e32 v14, v15, v14
	s_nop 0
	v_cndmask_b32_e64 v15, 0, 4, s[4:5]
	v_cmp_neq_f32_e64 s[4:5], 0, v17
	s_nop 1
	v_cndmask_b32_e64 v16, 0, 8, s[4:5]
	v_or3_b32 v14, v14, v15, v16
	s_nop 1
	v_mov_b32_dpp v15, v14 quad_perm:[1,0,3,2] row_mask:0xf bank_mask:0xf
	v_lshl_or_b32 v14, v15, 4, v14
	v_mov_b32_e32 v45, v14
	s_waitcnt vmcnt(2)
	v_cmp_neq_f32_e64 s[4:5], 0, v10
	s_nop 1
	v_cndmask_b32_e64 v10, 0, 1, s[4:5]
	v_cmp_neq_f32_e64 s[4:5], 0, v11
	s_nop 1
	v_cndmask_b32_e64 v11, 0, 2, s[4:5]
	v_cmp_neq_f32_e64 s[4:5], 0, v12
	v_or_b32_e32 v10, v11, v10
	s_nop 0
	v_cndmask_b32_e64 v11, 0, 4, s[4:5]
	v_cmp_neq_f32_e64 s[4:5], 0, v13
	s_nop 1
	v_cndmask_b32_e64 v12, 0, 8, s[4:5]
	v_or3_b32 v10, v10, v11, v12
	s_nop 1
	v_mov_b32_dpp v11, v10 quad_perm:[1,0,3,2] row_mask:0xf bank_mask:0xf
	v_lshl_or_b32 v10, v11, 4, v10
	v_lshl_or_b32 v45, v10, 8, v45
	s_waitcnt vmcnt(1)
	v_cmp_neq_f32_e64 s[4:5], 0, v6
	s_nop 1
	v_cndmask_b32_e64 v6, 0, 1, s[4:5]
	v_cmp_neq_f32_e64 s[4:5], 0, v7
	s_nop 1
	v_cndmask_b32_e64 v7, 0, 2, s[4:5]
	v_cmp_neq_f32_e64 s[4:5], 0, v8
	v_or_b32_e32 v6, v7, v6
	s_nop 0
	v_cndmask_b32_e64 v7, 0, 4, s[4:5]
	v_cmp_neq_f32_e64 s[4:5], 0, v9
	s_nop 1
	v_cndmask_b32_e64 v8, 0, 8, s[4:5]
	v_or3_b32 v6, v6, v7, v8
	s_nop 1
	v_mov_b32_dpp v7, v6 quad_perm:[1,0,3,2] row_mask:0xf bank_mask:0xf
	v_lshl_or_b32 v6, v7, 4, v6
	v_lshl_or_b32 v45, v6, 16, v45
	s_waitcnt vmcnt(0)
	v_cmp_neq_f32_e64 s[4:5], 0, v2
	s_nop 1
	v_cndmask_b32_e64 v2, 0, 1, s[4:5]
	v_cmp_neq_f32_e64 s[4:5], 0, v3
	s_nop 1
	v_cndmask_b32_e64 v3, 0, 2, s[4:5]
	v_cmp_neq_f32_e64 s[4:5], 0, v4
	v_or_b32_e32 v2, v3, v2
	s_nop 0
	v_cndmask_b32_e64 v3, 0, 4, s[4:5]
	v_cmp_neq_f32_e64 s[4:5], 0, v5
	s_nop 1
	v_cndmask_b32_e64 v4, 0, 8, s[4:5]
	v_or3_b32 v2, v2, v3, v4
	s_nop 1
	v_mov_b32_dpp v3, v2 quad_perm:[1,0,3,2] row_mask:0xf bank_mask:0xf
	v_lshl_or_b32 v2, v3, 4, v2
	v_lshl_or_b32 v45, v2, 24, v45
	s_and_saveexec_b64 s[4:5], vcc
	ds_write_b64 v34, v[44:45]
	s_or_b64 exec, exec, s[4:5]
	v_lshlrev_b32_e32 v2, 8, v31
	v_add3_u32 v2, v32, v2, v30
	s_waitcnt lgkmcnt(0)
	s_barrier
	ds_read_i8 v3, v2
	ds_read_i8 v4, v2 offset:64
	ds_read_i8 v5, v2 offset:128
	ds_read_i8 v2, v2 offset:192
	v_cmp_gt_u32_e64 s[68:69], 32, v30
	s_waitcnt lgkmcnt(3)
	v_and_b32_e32 v6, 1, v3
	v_cmp_ne_u32_e64 s[64:65], 0, v6
	v_bfe_u32 v6, v3, 1, 1
	v_cmp_ne_u32_e64 s[62:63], 0, v6
	v_bfe_u32 v6, v3, 2, 1
	v_cmp_ne_u32_e64 s[60:61], 0, v6
	v_bfe_u32 v6, v3, 3, 1
	v_cmp_ne_u32_e64 s[58:59], 0, v6
	v_bfe_u32 v6, v3, 4, 1
	v_cmp_ne_u32_e64 s[56:57], 0, v6
	v_bfe_u32 v6, v3, 5, 1
	v_cmp_ne_u32_e64 s[54:55], 0, v6
	v_bfe_u32 v6, v3, 6, 1
	v_cmp_gt_i16_e64 s[50:51], 0, v3
	s_waitcnt lgkmcnt(2)
	v_and_b32_e32 v3, 1, v4
	v_cmp_ne_u32_e64 s[48:49], 0, v3
	v_bfe_u32 v3, v4, 1, 1
	v_cmp_ne_u32_e64 s[46:47], 0, v3
	v_bfe_u32 v3, v4, 2, 1
	v_cmp_ne_u32_e64 s[44:45], 0, v3
	v_bfe_u32 v3, v4, 3, 1
	v_cmp_ne_u32_e64 s[42:43], 0, v3
	v_bfe_u32 v3, v4, 4, 1
	v_cmp_ne_u32_e64 s[40:41], 0, v3
	v_bfe_u32 v3, v4, 5, 1
	v_cmp_ne_u32_e64 s[38:39], 0, v3
	v_bfe_u32 v3, v4, 6, 1
	v_cmp_ne_u32_e64 s[36:37], 0, v3
	s_waitcnt lgkmcnt(1)
	v_and_b32_e32 v3, 1, v5
	v_cmp_ne_u32_e64 s[30:31], 0, v3
	v_bfe_u32 v3, v5, 1, 1
	v_cmp_ne_u32_e64 s[28:29], 0, v3
	v_bfe_u32 v3, v5, 2, 1
	v_cmp_ne_u32_e64 s[26:27], 0, v3
	v_bfe_u32 v3, v5, 3, 1
	v_cmp_ne_u32_e64 s[24:25], 0, v3
	v_bfe_u32 v3, v5, 4, 1
	v_cmp_ne_u32_e64 s[22:23], 0, v3
	v_bfe_u32 v3, v5, 5, 1
	v_cmp_ne_u32_e64 s[20:21], 0, v3
	v_bfe_u32 v3, v5, 6, 1
	v_cmp_ne_u32_e64 s[18:19], 0, v3
	s_waitcnt lgkmcnt(0)
	v_and_b32_e32 v3, 1, v2
	v_cmp_ne_u32_e64 s[14:15], 0, v3
	v_bfe_u32 v3, v2, 1, 1
	v_cmp_ne_u32_e64 s[12:13], 0, v3
	v_bfe_u32 v3, v2, 2, 1
	v_cmp_ne_u32_e64 s[10:11], 0, v3
	v_bfe_u32 v3, v2, 3, 1
	v_cmp_ne_u32_e64 s[8:9], 0, v3
	v_bfe_u32 v3, v2, 4, 1
	v_cmp_ne_u32_e64 s[6:7], 0, v3
	v_bfe_u32 v3, v2, 5, 1
	v_cmp_ne_u32_e64 s[4:5], 0, v3
	v_bfe_u32 v3, v2, 6, 1
	v_cmp_ne_u32_e64 s[52:53], 0, v6
	v_cmp_gt_i16_e64 s[34:35], 0, v4
	v_cmp_gt_i16_e64 s[16:17], 0, v5
	v_cmp_ne_u32_e64 s[66:67], 0, v3
	v_cmp_gt_i16_e32 vcc, 0, v2
	s_and_saveexec_b64 s[78:79], s[68:69]
	s_cbranch_execz .LBB0_42
	v_cmp_eq_u32_e64 s[68:69], 0, v30
	v_mov_b32_e32 v3, s65
	v_mov_b32_e32 v2, s64
	v_cndmask_b32_e64 v3, 0, v3, s[68:69]
	v_mov_b32_e32 v4, s63
	v_cmp_eq_u32_e64 s[64:65], 1, v30
	v_cndmask_b32_e64 v2, 0, v2, s[68:69]
	s_load_dwordx2 s[80:81], s[0:1], 0x8
	v_cndmask_b32_e64 v3, v3, v4, s[64:65]
	v_mov_b32_e32 v4, s62
	v_cndmask_b32_e64 v2, v2, v4, s[64:65]
	v_mov_b32_e32 v4, s60
	v_cmp_eq_u32_e64 s[62:63], 2, v30
	s_ashr_i32 s77, s76, 31
	v_lshlrev_b32_e32 v1, 4, v1
	v_cndmask_b32_e64 v2, v2, v4, s[62:63]
	v_mov_b32_e32 v4, s61
	v_cndmask_b32_e64 v3, v3, v4, s[62:63]
	v_mov_b32_e32 v4, s59
	v_cmp_eq_u32_e64 s[60:61], 3, v30
	v_lshlrev_b32_e32 v6, 3, v30
	v_mov_b32_e32 v7, 0
	v_cndmask_b32_e64 v3, v3, v4, s[60:61]
	v_mov_b32_e32 v4, s58
	v_cndmask_b32_e64 v2, v2, v4, s[60:61]
	v_mov_b32_e32 v4, s56
	v_cmp_eq_u32_e64 s[58:59], 4, v30
	s_nop 1
	v_cndmask_b32_e64 v2, v2, v4, s[58:59]
	v_mov_b32_e32 v4, s57
	v_cndmask_b32_e64 v3, v3, v4, s[58:59]
	v_mov_b32_e32 v4, s55
	v_cmp_eq_u32_e64 s[56:57], 5, v30
	s_nop 1
	v_cndmask_b32_e64 v3, v3, v4, s[56:57]
	v_mov_b32_e32 v4, s54
	v_cndmask_b32_e64 v2, v2, v4, s[56:57]
	v_mov_b32_e32 v4, s52
	v_cmp_eq_u32_e64 s[54:55], 6, v30
	s_nop 1
	v_cndmask_b32_e64 v2, v2, v4, s[54:55]
	v_mov_b32_e32 v4, s53
	v_cndmask_b32_e64 v3, v3, v4, s[54:55]
	v_mov_b32_e32 v4, s51
	v_cmp_eq_u32_e64 s[52:53], 7, v30
	s_nop 1
	v_cndmask_b32_e64 v3, v3, v4, s[52:53]
	v_mov_b32_e32 v4, s50
	v_cndmask_b32_e64 v2, v2, v4, s[52:53]
	v_mov_b32_e32 v4, s48
	v_cmp_eq_u32_e64 s[50:51], 8, v30
	s_nop 1
	v_cndmask_b32_e64 v2, v2, v4, s[50:51]
	v_mov_b32_e32 v4, s49
	v_cndmask_b32_e64 v3, v3, v4, s[50:51]
	v_mov_b32_e32 v4, s47
	v_cmp_eq_u32_e64 s[48:49], 9, v30
	s_nop 1
	v_cndmask_b32_e64 v3, v3, v4, s[48:49]
	v_mov_b32_e32 v4, s46
	v_cndmask_b32_e64 v2, v2, v4, s[48:49]
	v_mov_b32_e32 v4, s44
	v_cmp_eq_u32_e64 s[46:47], 10, v30
	s_nop 1
	v_cndmask_b32_e64 v2, v2, v4, s[46:47]
	v_mov_b32_e32 v4, s45
	v_cndmask_b32_e64 v3, v3, v4, s[46:47]
	v_mov_b32_e32 v4, s43
	v_cmp_eq_u32_e64 s[44:45], 11, v30
	s_nop 1
	v_cndmask_b32_e64 v3, v3, v4, s[44:45]
	v_mov_b32_e32 v4, s42
	v_cndmask_b32_e64 v2, v2, v4, s[44:45]
	v_mov_b32_e32 v4, s40
	v_cmp_eq_u32_e64 s[42:43], 12, v30
	s_nop 1
	v_cndmask_b32_e64 v2, v2, v4, s[42:43]
	v_mov_b32_e32 v4, s41
	v_cndmask_b32_e64 v3, v3, v4, s[42:43]
	v_mov_b32_e32 v4, s39
	v_cmp_eq_u32_e64 s[40:41], 13, v30
	s_nop 1
	v_cndmask_b32_e64 v3, v3, v4, s[40:41]
	v_mov_b32_e32 v4, s38
	v_cndmask_b32_e64 v2, v2, v4, s[40:41]
	v_mov_b32_e32 v4, s36
	v_cmp_eq_u32_e64 s[38:39], 14, v30
	s_nop 1
	v_cndmask_b32_e64 v2, v2, v4, s[38:39]
	v_mov_b32_e32 v4, s37
	v_cndmask_b32_e64 v3, v3, v4, s[38:39]
	v_mov_b32_e32 v4, s35
	v_cmp_eq_u32_e64 s[36:37], 15, v30
	s_nop 1
	v_cndmask_b32_e64 v3, v3, v4, s[36:37]
	v_mov_b32_e32 v4, s34
	v_cndmask_b32_e64 v2, v2, v4, s[36:37]
	v_mov_b32_e32 v4, s30
	v_cmp_eq_u32_e64 s[34:35], 16, v30
	s_nop 1
	v_cndmask_b32_e64 v2, v2, v4, s[34:35]
	v_mov_b32_e32 v4, s31
	v_cndmask_b32_e64 v3, v3, v4, s[34:35]
	v_mov_b32_e32 v4, s29
	v_cmp_eq_u32_e64 s[30:31], 17, v30
	s_nop 1
	v_cndmask_b32_e64 v3, v3, v4, s[30:31]
	v_mov_b32_e32 v4, s28
	v_cndmask_b32_e64 v2, v2, v4, s[30:31]
	v_mov_b32_e32 v4, s26
	v_cmp_eq_u32_e64 s[28:29], 18, v30
	s_nop 1
	v_cndmask_b32_e64 v2, v2, v4, s[28:29]
	v_mov_b32_e32 v4, s27
	v_cndmask_b32_e64 v3, v3, v4, s[28:29]
	v_mov_b32_e32 v4, s25
	v_cmp_eq_u32_e64 s[26:27], 19, v30
	s_nop 1
	v_cndmask_b32_e64 v3, v3, v4, s[26:27]
	v_mov_b32_e32 v4, s24
	v_cndmask_b32_e64 v2, v2, v4, s[26:27]
	v_mov_b32_e32 v4, s22
	v_cmp_eq_u32_e64 s[24:25], 20, v30
	s_nop 1
	v_cndmask_b32_e64 v2, v2, v4, s[24:25]
	v_mov_b32_e32 v4, s23
	v_cndmask_b32_e64 v3, v3, v4, s[24:25]
	v_mov_b32_e32 v4, s21
	v_cmp_eq_u32_e64 s[22:23], 21, v30
	s_nop 1
	v_cndmask_b32_e64 v3, v3, v4, s[22:23]
	v_mov_b32_e32 v4, s20
	v_cndmask_b32_e64 v2, v2, v4, s[22:23]
	v_mov_b32_e32 v4, s18
	v_cmp_eq_u32_e64 s[20:21], 22, v30
	s_nop 1
	v_cndmask_b32_e64 v2, v2, v4, s[20:21]
	v_mov_b32_e32 v4, s19
	v_cndmask_b32_e64 v3, v3, v4, s[20:21]
	v_mov_b32_e32 v4, s17
	v_cmp_eq_u32_e64 s[18:19], 23, v30
	s_nop 1
	v_cndmask_b32_e64 v3, v3, v4, s[18:19]
	v_mov_b32_e32 v4, s16
	v_cndmask_b32_e64 v2, v2, v4, s[18:19]
	v_mov_b32_e32 v4, s14
	v_cmp_eq_u32_e64 s[16:17], 24, v30
	s_nop 1
	v_cndmask_b32_e64 v2, v2, v4, s[16:17]
	v_mov_b32_e32 v4, s15
	v_cndmask_b32_e64 v3, v3, v4, s[16:17]
	v_mov_b32_e32 v4, s13
	v_cmp_eq_u32_e64 s[14:15], 25, v30
	s_nop 1
	v_cndmask_b32_e64 v3, v3, v4, s[14:15]
	v_mov_b32_e32 v4, s12
	v_cndmask_b32_e64 v2, v2, v4, s[14:15]
	v_mov_b32_e32 v4, s10
	v_cmp_eq_u32_e64 s[12:13], 26, v30
	s_nop 1
	v_cndmask_b32_e64 v2, v2, v4, s[12:13]
	v_mov_b32_e32 v4, s11
	v_cndmask_b32_e64 v3, v3, v4, s[12:13]
	v_mov_b32_e32 v4, s9
	v_cmp_eq_u32_e64 s[10:11], 27, v30
	s_nop 1
	v_cndmask_b32_e64 v3, v3, v4, s[10:11]
	v_mov_b32_e32 v4, s8
	v_cndmask_b32_e64 v2, v2, v4, s[10:11]
	v_mov_b32_e32 v4, s6
	v_cmp_eq_u32_e64 s[8:9], 28, v30
	s_nop 1
	v_cndmask_b32_e64 v2, v2, v4, s[8:9]
	v_mov_b32_e32 v4, s7
	v_cndmask_b32_e64 v3, v3, v4, s[8:9]
	v_mov_b32_e32 v4, s5
	v_cmp_eq_u32_e64 s[6:7], 29, v30
	s_nop 1
	v_cndmask_b32_e64 v3, v3, v4, s[6:7]
	v_mov_b32_e32 v4, s4
	v_cndmask_b32_e64 v2, v2, v4, s[6:7]
	v_mov_b32_e32 v4, s66
	v_cmp_eq_u32_e64 s[4:5], 30, v30
	s_nop 1
	v_cndmask_b32_e64 v2, v2, v4, s[4:5]
	v_mov_b32_e32 v4, s67
	v_cndmask_b32_e64 v3, v3, v4, s[4:5]
	v_mov_b32_e32 v4, vcc_hi
	v_cmp_eq_u32_e64 s[4:5], 31, v30
	s_nop 1
	v_cndmask_b32_e64 v3, v3, v4, s[4:5]
	v_mov_b32_e32 v4, vcc_lo
	v_cndmask_b32_e64 v2, v2, v4, s[4:5]
	s_lshl_b64 s[4:5], s[76:77], 9
	v_lshlrev_b32_e32 v4, 2, v31
	v_or3_b32 v4, s4, v1, v4
	v_mov_b32_e32 v5, s5
	v_lshlrev_b64 v[4:5], 6, v[4:5]
	s_waitcnt lgkmcnt(0)
	v_lshl_add_u64 v[4:5], s[80:81], 0, v[4:5]
	v_lshl_add_u64 v[4:5], v[4:5], 0, v[6:7]
	global_store_dwordx2 v[4:5], v[2:3], off sc0 sc1
	s_nop 0
